# k_fine: wait for the loff entry after the lane-index setup and LDS clear instead of before (load latency overlapped)
# speedup vs baseline: 1.0043x; 1.0043x over previous
_Z6k_finePKjPKtPiPt:
	s_movk_i32 s3, 0x100
	v_cmp_gt_u32_e32 vcc, s3, v0
	v_mov_b32_e32 v26, 0
	v_mov_b32_e32 v8, 0
	s_and_saveexec_b64 s[4:5], vcc
	s_cbranch_execz .LBB0_2
	s_load_dwordx2 s[6:7], s[0:1], 0x8
	s_movk_i32 s3, 0x188
	v_mov_b32_e32 v1, s2
	v_mad_u32_u24 v2, v0, s3, v1
	v_ashrrev_i32_e32 v3, 31, v2
	s_waitcnt lgkmcnt(0)
	v_lshl_add_u64 v[2:3], v[2:3], 1, s[6:7]
	global_load_dword v55, v[2:3], off
.LBB0_2:
	s_or_b64 exec, exec, s[4:5]
	s_movk_i32 s3, 0x80
	v_cmp_gt_u32_e64 s[28:29], s3, v0
	s_and_saveexec_b64 s[4:5], s[28:29]
	v_lshlrev_b32_e32 v1, 2, v0
	v_mov_b32_e32 v2, 0
	ds_write_b32 v1, v2 offset:31744
	s_or_b64 exec, exec, s[4:5]
	v_mbcnt_lo_u32_b32 v1, -1, 0
	v_mbcnt_hi_u32_b32 v3, -1, v1
	v_and_b32_e32 v4, 64, v3
	v_add_u32_e32 v1, -1, v3
	v_cmp_lt_i32_e64 s[4:5], v1, v4
	v_add_u32_e32 v5, -2, v3
	v_lshrrev_b32_e32 v35, 6, v0
	v_cndmask_b32_e64 v1, v1, v3, s[4:5]
	v_lshlrev_b32_e32 v31, 2, v1
	v_and_b32_e32 v1, 63, v0
	v_cmp_eq_u32_e64 s[36:37], 0, v1
	v_cmp_lt_i32_e64 s[4:5], v5, v4
	s_waitcnt lgkmcnt(0)
	v_cndmask_b32_e64 v5, v5, v3, s[4:5]
	v_lshlrev_b32_e32 v32, 2, v5
	v_cmp_gt_u32_e64 s[4:5], 2, v1
	s_waitcnt lgkmcnt(0)
	s_nop 0
	v_add_u32_e32 v5, -4, v3
	v_cmp_lt_i32_e64 s[6:7], v5, v4
	s_nop 1
	v_cndmask_b32_e64 v5, v5, v3, s[6:7]
	v_lshlrev_b32_e32 v33, 2, v5
	v_cmp_gt_u32_e64 s[6:7], 4, v1
	s_waitcnt lgkmcnt(0)
	s_nop 0
	v_add_u32_e32 v5, -8, v3
	v_cmp_lt_i32_e64 s[8:9], v5, v4
	s_nop 1
	v_cndmask_b32_e64 v5, v5, v3, s[8:9]
	v_lshlrev_b32_e32 v34, 2, v5
	v_cmp_gt_u32_e64 s[8:9], 8, v1
	s_waitcnt lgkmcnt(0)
	s_nop 0
	v_add_u32_e32 v5, -16, v3
	v_cmp_lt_i32_e64 s[10:11], v5, v4
	s_nop 1
	v_cndmask_b32_e64 v5, v5, v3, s[10:11]
	v_lshlrev_b32_e32 v36, 2, v5
	v_cmp_gt_u32_e64 s[10:11], 16, v1
	s_waitcnt lgkmcnt(0)
	s_nop 0
	v_subrev_u32_e32 v5, 32, v3
	v_cmp_lt_i32_e64 s[12:13], v5, v4
	s_nop 1
	v_cndmask_b32_e64 v3, v5, v3, s[12:13]
	v_lshlrev_b32_e32 v37, 2, v3
	s_waitcnt vmcnt(0)
	v_and_b32_e32 v8, 0xffff, v55
	v_sub_u32_sdwa v26, v55, v8 dst_sel:DWORD dst_unused:UNUSED_PAD src0_sel:WORD_1 src1_sel:DWORD
	v_cndmask_b32_e32 v8, 0, v8, vcc
	v_cndmask_b32_e32 v26, 0, v26, vcc
	v_mov_b32_e32 v2, v8
	s_nop 1
	v_add_u32_dpp v2, v2, v2 row_shr:1 row_mask:0xf bank_mask:0xf bound_ctrl:1
	s_nop 1
	v_add_u32_dpp v2, v2, v2 row_shr:2 row_mask:0xf bank_mask:0xf bound_ctrl:1
	s_nop 1
	v_add_u32_dpp v2, v2, v2 row_shr:4 row_mask:0xf bank_mask:0xf bound_ctrl:1
	s_nop 1
	v_add_u32_dpp v2, v2, v2 row_shr:8 row_mask:0xf bank_mask:0xf bound_ctrl:1
	s_nop 1
	v_add_u32_dpp v2, v2, v2 row_bcast:15 row_mask:0xa bank_mask:0xf
	s_nop 1
	v_add_u32_dpp v2, v2, v2 row_bcast:31 row_mask:0xc bank_mask:0xf
	v_mov_b32_e32 v3, 0
	v_cmp_eq_u32_e64 s[12:13], 63, v1
	s_and_saveexec_b64 s[14:15], s[12:13]
	s_cbranch_execz .LBB0_6
	v_lshlrev_b32_e32 v4, 2, v35
	s_waitcnt lgkmcnt(0)
	v_add_u32_e32 v2, v2, v3
	ds_write_b32 v4, v2 offset:32256
